# v24 + static s_setprio 1 for waves 4-7 during the dilated-attention item loop
# baseline (speedup 1.0000x reference)
.LBB0_286:
	s_or_b64 exec, exec, s[4:5]
	s_ashr_i32 s5, s7, 9
	s_and_b32 s24, s5, -2
	s_ashr_i32 s75, s7, 6
	s_lshr_b32 s5, 16, s24
	s_and_b32 s74, s6, 3
	s_ashr_i32 s4, s3, 3
	s_and_b32 s3, s75, 15
	s_sub_i32 s6, 4, s24
	s_add_i32 s5, s5, -1
	s_lshr_b32 s25, s3, s6
	s_and_b32 s3, s5, s3
	s_ashr_i32 s5, s4, 31
	s_lshl_b64 s[20:21], s[4:5], 12
	s_lshr_b32 s6, 0x400, s24
	s_or_b32 s4, s20, s25
	s_mul_i32 s6, s6, s74
	s_lshl_b32 s3, s3, 6
	s_mul_hi_u32 s26, s4, 0x1800
	s_mul_i32 s76, s21, 0x1800
	s_add_i32 s3, s3, s6
	s_lshl_b64 s[22:23], 8, s24
	s_mul_i32 s25, s4, 0x1800
	s_add_i32 s26, s26, s76
	s_add_u32 s25, s10, s25
	s_addc_u32 s26, s11, s26
	s_lshl_b32 s27, s16, 6
	s_lshl_b32 s16, s16, 7
	s_add_u32 s25, s25, s16
	v_sub_co_u32_e64 v2, s[6:7], s3, 64
	s_addc_u32 s26, s26, 0
	s_and_b64 s[6:7], s[6:7], exec
	v_readfirstlane_b32 s6, v2
	s_cselect_b32 s6, s3, s6
	s_ashr_i32 s7, s6, 31
	s_lshl_b64 s[6:7], s[6:7], s24
	v_bfe_u32 v3, v0, 3, 3
	s_mulk_i32 s7, 0x1800
	s_mul_hi_u32 s28, s6, 0x1800
	v_lshlrev_b32_e32 v3, s24, v3
	s_add_i32 s28, s28, s7
	s_mulk_i32 s6, 0x1800
	v_mul_lo_u32 v3, v3, s49
	v_lshlrev_b32_e32 v180, 3, v0
	s_add_u32 s6, s25, s6
	v_and_or_b32 v168, v180, 56, v3
	s_addc_u32 s7, s26, s28
	v_lshl_add_u64 v[2:3], v[168:169], 1, s[6:7]
	v_lshl_add_u64 v[4:5], v[2:3], 0, s[18:19]
	v_mad_u64_u32 v[6:7], s[6:7], s22, v172, v[4:5]
	s_mul_i32 s6, s23, 0x1800
	s_nop 0
	v_add_u32_e32 v7, s6, v7
	v_mad_u64_u32 v[8:9], s[6:7], s22, v173, v[4:5]
	s_mul_i32 s6, s23, 0x3000
	s_waitcnt lgkmcnt(0)
	s_barrier
	v_add_u32_e32 v9, s6, v9
	global_load_dwordx4 v[128:131], v[6:7], off
	global_load_dwordx4 v[132:135], v[8:9], off
	v_mad_u64_u32 v[6:7], s[6:7], s22, v174, v[4:5]
	s_mul_i32 s6, s23, 0x4800
	s_nop 0
	v_add_u32_e32 v7, s6, v7
	v_mad_u64_u32 v[8:9], s[6:7], s22, v175, v[4:5]
	s_mul_i32 s6, s23, 0x6000
	s_nop 0
	v_add_u32_e32 v9, s6, v9
	global_load_dwordx4 v[136:139], v[6:7], off
	global_load_dwordx4 v[140:143], v[8:9], off
	v_mad_u64_u32 v[6:7], s[6:7], s22, v176, v[4:5]
	s_mul_i32 s6, s23, 0x7800
	v_and_b32_e32 v1, 31, v0
	v_add_u32_e32 v7, s6, v7
	v_mad_u64_u32 v[8:9], s[6:7], s22, v177, v[4:5]
	s_mul_i32 s6, s23, 0x9000
	v_add_u32_e32 v168, s3, v1
	s_mov_b32 s5, s21
	v_add_u32_e32 v9, s6, v9
	global_load_dwordx4 v[144:147], v[6:7], off
	global_load_dwordx4 v[152:155], v[8:9], off
	v_mad_u64_u32 v[4:5], s[6:7], s22, v178, v[4:5]
	v_lshlrev_b64 v[6:7], s24, v[168:169]
	s_mul_i32 s6, s23, 0xa800
	v_lshl_add_u64 v[6:7], v[6:7], 0, s[4:5]
	v_add_u32_e32 v5, s6, v5
	v_mad_u64_u32 v[8:9], s[6:7], v6, s56, v[170:171]
	v_mov_b32_e32 v6, v9
	v_mad_u64_u32 v[6:7], s[6:7], v7, s56, v[6:7]
	v_add_co_u32_e32 v2, vcc, s57, v2
	v_mov_b32_e32 v9, v6
	v_lshrrev_b32_e32 v1, 1, v0
	v_addc_co_u32_e32 v3, vcc, 0, v3, vcc
	v_lshl_add_u64 v[6:7], v[8:9], 0, s[16:17]
	v_and_b32_e32 v8, 16, v1
	v_mov_b32_e32 v9, v169
	v_add_u32_e32 v168, 32, v168
	v_lshl_add_u64 v[6:7], v[6:7], 0, v[8:9]
	global_load_dwordx4 v[148:151], v[2:3], off
	global_load_dwordx4 v[96:99], v[6:7], off offset:3072
	global_load_dwordx4 v[100:103], v[6:7], off offset:3104
	global_load_dwordx4 v[104:107], v[6:7], off offset:3136
	v_lshlrev_b64 v[2:3], s24, v[168:169]
	v_lshl_add_u64 v[2:3], v[2:3], 0, s[4:5]
	v_mad_u64_u32 v[10:11], s[4:5], v2, s56, v[170:171]
	v_mov_b32_e32 v2, v11
	v_mad_u64_u32 v[2:3], s[4:5], v3, s56, v[2:3]
	v_mov_b32_e32 v11, v2
	v_lshl_add_u64 v[2:3], v[10:11], 0, s[16:17]
	v_lshl_add_u64 v[2:3], v[2:3], 0, v[8:9]
	global_load_dwordx4 v[108:111], v[6:7], off offset:3168
	global_load_dwordx4 v[112:115], v[2:3], off offset:3072
	global_load_dwordx4 v[116:119], v[2:3], off offset:3104
	global_load_dwordx4 v[120:123], v[2:3], off offset:3136
	global_load_dwordx4 v[156:159], v[4:5], off
	global_load_dwordx4 v[124:127], v[2:3], off offset:3168
	s_lshl_b32 s3, s75, 8
	s_lshl_b32 s4, s75, 13
	s_add_i32 s79, s4, 0
	s_add_i32 s81, s3, 0
	s_add_i32 s80, s79, 0x10000
	s_add_i32 s81, s81, 0x21000
	s_add_u32 s22, s10, s16
	v_and_b32_e32 v181, 63, v0
	s_mov_b32 s78, 0
	s_addc_u32 s23, s11, 0
	s_lshl_b32 s77, s27, 1
	s_cmp_lt_u32 s75, 4
	s_cbranch_scc1 .Ldil_nostag
	s_sleep 32
	s_setprio 1

.LBB0_341:
	s_setprio 0
	s_lshl_b32 s3, s74, 10
	s_or_b32 s20, s20, s3
	s_waitcnt vmcnt(0)
	s_barrier
	s_waitcnt vmcnt(0)
	buffer_inv sc1
	s_waitcnt vmcnt(0)
	v_and_b32_e32 v2, 56, v180
	s_add_u32 s4, s46, s77
	s_addc_u32 s5, s47, 0
	v_lshlrev_b32_e32 v168, 1, v2
	v_lshl_add_u64 v[0:1], s[4:5], 0, v[168:169]
	s_mov_b32 s3, 0
	v_lshlrev_b32_e32 v168, 1, v2
